# cvt3 prologue de-serialised: block-range counts hard-coded (one scalar pointer load instead of a chain of 2-3 dependent scalar loads per block)
# speedup vs baseline: 1.0207x; 1.0171x over previous
_Z8cvt3_f16PKfPDF16_iS0_S1_iS0_S1_iPfS2_:
	s_cmpk_gt_i32 s2, 0x1ff
	s_mov_b64 s[4:5], -1
	s_cbranch_scc0 .LBB0_10
	s_movk_i32 s9, 0x800
	s_add_i32 s8, s2, 0xfffffe00
	s_cmp_lt_i32 s8, s9
	s_cbranch_scc1 .LBB0_5
	s_movk_i32 s3, 0x1400
	s_cmp_ge_i32 s8, s3
	s_cbranch_scc0 .LBB0_6
	s_sub_i32 s3, s8, s3
	s_cbranch_execz .LBB0_7
